# v63 without the wave 4-7 start delay in the weight-copy chunks (keeps softmax FMA, static priority, dropped store-ack wait)
# baseline (speedup 1.0000x reference)
.LBB6_1307:
	v_readlane_b32 s6, v254, 13
	v_readlane_b32 s7, v254, 14
	v_mov_b32_e32 v167, v0
	s_waitcnt lgkmcnt(0)
	s_barrier
	s_max_i32 s36, s90, 0
	v_readfirstlane_b32 s0, v167
	s_ashr_i32 s67, s0, 6
	v_readlane_b32 s0, v254, 60
	s_lshl_b32 s81, s67, 14
	v_readlane_b32 s1, v254, 61
	v_and_b32_e32 v166, 63, v167
	s_add_i32 s66, s81, 0
	s_mov_b64 s[2:3], -1
	s_and_b64 vcc, exec, s[0:1]
	s_cbranch_vccz .LBB6_1319
	s_min_i32 s28, s91, 0xdc00
	s_cmp_le_i32 s28, s36
	s_cbranch_scc1 .LBB6_1313
	s_sub_i32 s0, s28, s36
	s_mov_b32 s2, 18
	s_cmp_lt_i32 s0, 32
	s_cbranch_scc1 .LBB6_1313
	s_add_i32 s29, s67, s36
	s_cmp_ge_i32 s29, s28
	s_cbranch_scc1 .LBB6_1313
	s_ashr_i32 s3, s2, 31
	s_lshl_b64 s[0:1], s[2:3], 3
	s_add_u32 s0, s76, s0
	s_addc_u32 s1, s77, s1
	s_load_dwordx2 s[0:1], s[0:1], 0x0
	v_lshrrev_b32_e32 v4, 3, v166
	v_lshlrev_b32_e32 v2, 2, v166
	v_mul_u32_u24_e32 v5, 0x2c00, v4
	v_and_b32_e32 v6, 28, v2
	s_waitcnt lgkmcnt(0)
	s_add_u32 s30, s0, 0x10800000
	v_or_b32_e32 v2, v5, v6
	v_lshl_add_u32 v5, v6, 2, s66
	v_lshlrev_b32_e32 v6, 5, v166
	s_addc_u32 s31, s1, 0
	v_lshrrev_b32_e32 v135, 2, v166
	v_lshlrev_b32_e32 v132, 4, v166
	v_and_b32_e32 v132, 48, v132
	s_add_u32 s34, s6, 0x85280000
	v_mul_u32_u24_e32 v4, 0x84, v4
	v_mul_u32_u24_e32 v6, 0x84, v132
	v_lshlrev_b32_e32 v7, 2, v135
	v_and_b32_e32 v134, 31, v167
	s_addc_u32 s35, s7, 0
	v_lshlrev_b32_e32 v2, 2, v2
	v_add3_u32 v136, s66, v6, v7
	v_mov_b32_e32 v133, v3
	v_add_u32_e32 v137, v5, v4
